# v33 + in-proj K-loop: last 4 of the 6 LDS-DMA pieces of each tile's second load phase issued behind the following MFMA burst (wait vmcnt(8)->vmcnt(4))
# baseline (speedup 1.0000x reference)
; #define PG8_STAGE(bufoff, gbase, voff) do { _Pragma("unroll") for (int _i = 0; _i < 2; ++_i) \
;         __builtin_amdgcn_global_load_lds((const unsigned*)((const char*)(gbase) + (voff)[_i]), (LAS unsigned*)(lds + (bufoff) + ldsw + _i * 8192), 16, 0, 0); } while (0)
; #define PG8_LDA(dst, b, h) do { _Pragma("unroll") for (int m = 0; m < 4; ++m) _Pragma("unroll") for (int k = 0; k < 2; ++k) dst[m][k] = *(const LAS bf16x8*)(lds + PG8_SA(b, h) + aoff + m * 2048 + k * 1024); } while (0)
; #define PG8_LDB(dst, b, h) do { _Pragma("unroll") for (int n = 0; n < 2; ++n) _Pragma("unroll") for (int k = 0; k < 2; ++k) dst[n][k] = *(const LAS bf16x8*)(lds + PG8_SB(b, h) + boff + n * 2048 + k * 1024); } while (0)
; #define PG8_MMA(ai, bj, At, Bt) do { __builtin_amdgcn_s_setprio(1); _Pragma("unroll") for (int m = 0; m < 4; ++m) _Pragma("unroll") for (int n = 0; n < 2; ++n) _Pragma("unroll") for (int k = 0; k < 2; ++k) \
;         acc[ai][bj][m][n] = __builtin_amdgcn_mfma_f32_16x16x32_bf16(Bt[n][k], At[m][k], acc[ai][bj][m][n], 0, 0, 0); __builtin_amdgcn_s_setprio(0); } while (0)
; template <class Epi, class Sched>
; __device__ __forceinline__ void gemm_phase(LAS unsigned char* lds, const int tid, const char* Abase, const int K, const Sched& S, const Epi& E) {
;     ...
;         for (int t = 0; t < nt; t += 2) {
;             if constexpr (Epi::MID) { if (t == (nt >> 1)) E.mid(acc, ui, wr, fr, lds); }
;             const bool last = (t == nt - 2);
;             const char* a1 = Abase + (size_t)(t + 1) * kstep;
;             const char* a2 = last ? Abase : Abase + (size_t)(t + 2) * kstep; const char* b2 = last ? nB : cB + (size_t)(t + 2) * kstep;
;             const char* a3 = a2 + kstep; const char* b3 = b2 + kstep;
;             unsigned w2[2][2];
;             if (last) { const u32x4 q = *vslot; w2[0][0] = q.x; w2[0][1] = q.y; w2[1][0] = q.z; w2[1][1] = q.w; }
;             else { w2[0][0] = vc[0][0]; w2[0][1] = vc[0][1]; w2[1][0] = vc[1][0]; w2[1][1] = vc[1][1]; }
;             PG8_LDB(B0, 0, 0); PG8_LDB(B1, 0, 1); PG8_SCHED; PG8_LDA(At, 0, 0); PG8_STAGE(PG8_SA(1, 1), a1, vc[1]);
;             PG8_WAIT_V(8); PG8_WAIT_L(0); PG8_BAR; PG8_MMA(0, 0, At, B0); PG8_MMA(0, 1, At, B1); PG8_BAR; PG8_SCHED;
;             PG8_LDA(At, 0, 1); PG8_STAGE(PG8_SB(0, 0), b2, voffB); PG8_STAGE(PG8_SB(0, 1), b2 + hstep, voffB); PG8_STAGE(PG8_SA(0, 0), a2, w2[0]);
.LBB0_347:
	s_add_u32 s16, s12, 0x80
	s_addc_u32 s17, s13, 0
	s_and_b64 s[14:15], s[14:15], exec
	s_cselect_b32 s17, s31, s17
	s_cselect_b32 s16, s30, s16
	s_cselect_b32 s15, s61, s18
	s_cselect_b32 s14, s60, s7
	s_add_i32 s20, 0, 0x10000
	v_add_u32_e32 v145, s20, v147
	s_add_i32 s27, 0, 0x14000
	ds_read_b128 v[150:153], v145
	ds_read_b128 v[154:157], v145 offset:1024
	ds_read_b128 v[158:161], v145 offset:2048
	ds_read_b128 v[162:165], v145 offset:3072
	v_add_u32_e32 v145, s27, v147
	ds_read_b128 v[166:169], v145
	ds_read_b128 v[170:173], v145 offset:1024
	ds_read_b128 v[174:177], v145 offset:2048
	ds_read_b128 v[178:181], v145 offset:3072
	v_lshl_add_u64 v[186:187], s[12:13], 0, v[116:117]
	s_add_i32 m0, s71, 0xc000
	ds_read_b128 v[182:185], v148
	ds_read_b128 v[202:205], v148 offset:1024
	ds_read_b128 v[206:209], v148 offset:2048
	ds_read_b128 v[214:217], v148 offset:3072
	ds_read_b128 v[218:221], v148 offset:4096
	ds_read_b128 v[222:225], v148 offset:5120
	ds_read_b128 v[226:229], v148 offset:6144
	ds_read_b128 v[230:233], v148 offset:7168
	global_load_lds_dwordx4 v[186:187], off
	v_lshl_add_u64 v[186:187], s[12:13], 0, v[138:139]
	s_add_i32 m0, s71, 0xe000
	s_nop 0
	global_load_lds_dwordx4 v[186:187], off
	s_waitcnt vmcnt(8)
	s_waitcnt lgkmcnt(0)
	s_barrier
	s_setprio 1
	s_waitcnt lgkmcnt(0)
	v_mfma_f32_16x16x32_bf16 v[130:133], v[150:153], v[182:185], v[130:133]
	v_mfma_f32_16x16x32_bf16 v[126:129], v[158:161], v[182:185], v[126:129]
	v_mfma_f32_16x16x32_bf16 v[110:113], v[150:153], v[206:209], v[110:113]
	v_mfma_f32_16x16x32_bf16 v[106:109], v[158:161], v[206:209], v[106:109]
	v_mfma_f32_16x16x32_bf16 v[94:97], v[150:153], v[218:221], v[94:97]
	v_mfma_f32_16x16x32_bf16 v[90:93], v[158:161], v[218:221], v[90:93]
	v_mfma_f32_16x16x32_bf16 v[78:81], v[150:153], v[226:229], v[78:81]
	v_mfma_f32_16x16x32_bf16 v[74:77], v[158:161], v[226:229], v[74:77]
	v_mfma_f32_16x16x32_bf16 v[130:133], v[154:157], v[202:205], v[130:133]
	v_mfma_f32_16x16x32_bf16 v[126:129], v[162:165], v[202:205], v[126:129]
	v_mfma_f32_16x16x32_bf16 v[110:113], v[154:157], v[214:217], v[110:113]
	v_mfma_f32_16x16x32_bf16 v[106:109], v[162:165], v[214:217], v[106:109]
	v_mfma_f32_16x16x32_bf16 v[94:97], v[154:157], v[222:225], v[94:97]
	v_mfma_f32_16x16x32_bf16 v[90:93], v[162:165], v[222:225], v[90:93]
	v_mfma_f32_16x16x32_bf16 v[78:81], v[154:157], v[230:233], v[78:81]
	v_mfma_f32_16x16x32_bf16 v[74:77], v[162:165], v[230:233], v[74:77]
	s_setprio 0
	s_setprio 1
	v_mfma_f32_16x16x32_bf16 v[122:125], v[166:169], v[182:185], v[122:125]
	v_mfma_f32_16x16x32_bf16 v[118:121], v[174:177], v[182:185], v[118:121]
	v_mfma_f32_16x16x32_bf16 v[102:105], v[166:169], v[206:209], v[102:105]
	v_mfma_f32_16x16x32_bf16 v[98:101], v[174:177], v[206:209], v[98:101]
	v_mfma_f32_16x16x32_bf16 v[86:89], v[166:169], v[218:221], v[86:89]
	v_mfma_f32_16x16x32_bf16 v[82:85], v[174:177], v[218:221], v[82:85]
	v_mfma_f32_16x16x32_bf16 v[70:73], v[166:169], v[226:229], v[70:73]
	v_mfma_f32_16x16x32_bf16 v[66:69], v[174:177], v[226:229], v[66:69]
	v_mfma_f32_16x16x32_bf16 v[122:125], v[170:173], v[202:205], v[122:125]
	v_mfma_f32_16x16x32_bf16 v[118:121], v[178:181], v[202:205], v[118:121]
	v_mfma_f32_16x16x32_bf16 v[102:105], v[170:173], v[214:217], v[102:105]
	v_mfma_f32_16x16x32_bf16 v[98:101], v[178:181], v[214:217], v[98:101]
	v_mfma_f32_16x16x32_bf16 v[86:89], v[170:173], v[222:225], v[86:89]
	v_mfma_f32_16x16x32_bf16 v[82:85], v[178:181], v[222:225], v[82:85]
	v_mfma_f32_16x16x32_bf16 v[70:73], v[170:173], v[230:233], v[70:73]
	v_mfma_f32_16x16x32_bf16 v[66:69], v[178:181], v[230:233], v[66:69]
	s_setprio 0
	s_barrier
	s_add_i32 s20, s20, s70
	v_lshl_add_u64 v[186:187], s[14:15], 0, v[134:135]
	s_mov_b32 m0, s20
	ds_read_b128 v[182:185], v148 offset:16384
	ds_read_b128 v[202:205], v148 offset:17408
	ds_read_b128 v[206:209], v148 offset:18432
	ds_read_b128 v[214:217], v148 offset:19456
	ds_read_b128 v[218:221], v148 offset:20480
	ds_read_b128 v[222:225], v148 offset:21504
	ds_read_b128 v[226:229], v148 offset:22528
	ds_read_b128 v[230:233], v148 offset:23552
	global_load_lds_dwordx4 v[186:187], off
	s_add_i32 m0, s20, 0x2000
	s_add_u32 s20, s14, 0x40000
	v_lshl_add_u64 v[190:191], s[14:15], 0, v[136:137]
	s_addc_u32 s21, s15, 0
	s_add_i32 s27, s27, s70
	global_load_lds_dwordx4 v[190:191], off
	s_waitcnt vmcnt(4)
	s_waitcnt lgkmcnt(0)
	s_barrier
; #define PG8_STAGE(bufoff, gbase, voff) do { _Pragma("unroll") for (int _i = 0; _i < 2; ++_i) \
;         __builtin_amdgcn_global_load_lds((const unsigned*)((const char*)(gbase) + (voff)[_i]), (LAS unsigned*)(lds + (bufoff) + ldsw + _i * 8192), 16, 0, 0); } while (0)
; #define PG8_LDA(dst, b, h) do { _Pragma("unroll") for (int m = 0; m < 4; ++m) _Pragma("unroll") for (int k = 0; k < 2; ++k) dst[m][k] = *(const LAS bf16x8*)(lds + PG8_SA(b, h) + aoff + m * 2048 + k * 1024); } while (0)
; #define PG8_LDB(dst, b, h) do { _Pragma("unroll") for (int n = 0; n < 2; ++n) _Pragma("unroll") for (int k = 0; k < 2; ++k) dst[n][k] = *(const LAS bf16x8*)(lds + PG8_SB(b, h) + boff + n * 2048 + k * 1024); } while (0)
; #define PG8_MMA(ai, bj, At, Bt) do { __builtin_amdgcn_s_setprio(1); _Pragma("unroll") for (int m = 0; m < 4; ++m) _Pragma("unroll") for (int n = 0; n < 2; ++n) _Pragma("unroll") for (int k = 0; k < 2; ++k) \
;         acc[ai][bj][m][n] = __builtin_amdgcn_mfma_f32_16x16x32_bf16(Bt[n][k], At[m][k], acc[ai][bj][m][n], 0, 0, 0); __builtin_amdgcn_s_setprio(0); } while (0)
; #define PG8_WAIT_V(n) asm volatile("s_waitcnt vmcnt(" #n ")" ::: "memory")
; #define PG8_WAIT_L(n) asm volatile("s_waitcnt lgkmcnt(" #n ")" ::: "memory")
; #define PG8_BAR __builtin_amdgcn_s_barrier()
; #define PG8_SCHED __builtin_amdgcn_sched_barrier(0)
; template <class Epi, class Sched>
; __device__ __forceinline__ void gemm_phase(LAS unsigned char* lds, const int tid, const char* Abase, const int K, const Sched& S, const Epi& E) {
;     ...
;             PG8_WAIT_V(8); PG8_WAIT_L(0); PG8_BAR; PG8_MMA(1, 0, At, B0); PG8_MMA(1, 1, At, B1); PG8_BAR; PG8_SCHED;
;             PG8_LDB(B0, 1, 0); PG8_LDB(B1, 1, 1); PG8_SCHED; PG8_LDA(At, 1, 0); PG8_STAGE(PG8_SA(0, 1), a2, w2[1]);
;             PG8_WAIT_V(8); PG8_WAIT_L(0); PG8_BAR; PG8_MMA(0, 0, At, B0); PG8_MMA(0, 1, At, B1); PG8_BAR; PG8_SCHED;
	s_setprio 1
	s_waitcnt lgkmcnt(0)
	v_mfma_f32_16x16x32_bf16 v[62:65], v[150:153], v[182:185], v[62:65]
	v_mfma_f32_16x16x32_bf16 v[58:61], v[158:161], v[182:185], v[58:61]
	v_mfma_f32_16x16x32_bf16 v[46:49], v[150:153], v[206:209], v[46:49]
	v_mfma_f32_16x16x32_bf16 v[42:45], v[158:161], v[206:209], v[42:45]
	v_mfma_f32_16x16x32_bf16 v[30:33], v[150:153], v[218:221], v[30:33]
	v_mfma_f32_16x16x32_bf16 v[26:29], v[158:161], v[218:221], v[26:29]
	v_mfma_f32_16x16x32_bf16 v[14:17], v[150:153], v[226:229], v[14:17]
	v_mfma_f32_16x16x32_bf16 v[10:13], v[158:161], v[226:229], v[10:13]
	v_mfma_f32_16x16x32_bf16 v[62:65], v[154:157], v[202:205], v[62:65]
	v_mfma_f32_16x16x32_bf16 v[58:61], v[162:165], v[202:205], v[58:61]
	v_mfma_f32_16x16x32_bf16 v[46:49], v[154:157], v[214:217], v[46:49]
	v_mfma_f32_16x16x32_bf16 v[42:45], v[162:165], v[214:217], v[42:45]
	v_mfma_f32_16x16x32_bf16 v[30:33], v[154:157], v[222:225], v[30:33]
	v_mfma_f32_16x16x32_bf16 v[26:29], v[162:165], v[222:225], v[26:29]
	v_mfma_f32_16x16x32_bf16 v[14:17], v[154:157], v[230:233], v[14:17]
	v_mfma_f32_16x16x32_bf16 v[10:13], v[162:165], v[230:233], v[10:13]
	s_setprio 0
	s_setprio 1
	v_mfma_f32_16x16x32_bf16 v[54:57], v[166:169], v[182:185], v[54:57]
	v_mfma_f32_16x16x32_bf16 v[50:53], v[174:177], v[182:185], v[50:53]
	v_mfma_f32_16x16x32_bf16 v[38:41], v[166:169], v[206:209], v[38:41]
	v_mfma_f32_16x16x32_bf16 v[34:37], v[174:177], v[206:209], v[34:37]
	v_mfma_f32_16x16x32_bf16 v[22:25], v[166:169], v[218:221], v[22:25]
	v_mfma_f32_16x16x32_bf16 v[18:21], v[174:177], v[218:221], v[18:21]
	v_mfma_f32_16x16x32_bf16 v[6:9], v[166:169], v[226:229], v[6:9]
	v_mfma_f32_16x16x32_bf16 v[2:5], v[174:177], v[226:229], v[2:5]
	v_mfma_f32_16x16x32_bf16 v[54:57], v[170:173], v[202:205], v[54:57]
	v_mfma_f32_16x16x32_bf16 v[50:53], v[178:181], v[202:205], v[50:53]
	v_mfma_f32_16x16x32_bf16 v[38:41], v[170:173], v[214:217], v[38:41]
	v_mfma_f32_16x16x32_bf16 v[34:37], v[178:181], v[214:217], v[34:37]
	v_mfma_f32_16x16x32_bf16 v[22:25], v[170:173], v[222:225], v[22:25]
	v_mfma_f32_16x16x32_bf16 v[18:21], v[178:181], v[222:225], v[18:21]
	v_mfma_f32_16x16x32_bf16 v[6:9], v[170:173], v[230:233], v[6:9]
	v_mfma_f32_16x16x32_bf16 v[2:5], v[178:181], v[230:233], v[2:5]
	s_setprio 0
	v_lshl_add_u64 v[192:193], s[20:21], 0, v[134:135]
	s_mov_b32 m0, s27
	v_mov_b32_e32 v145, v1
	global_load_lds_dwordx4 v[192:193], off
	v_lshl_add_u64 v[192:193], s[20:21], 0, v[136:137]
	s_add_i32 m0, s27, 0x2000
	s_nop 0
	global_load_lds_dwordx4 v[192:193], off
	s_mov_b32 m0, s71
	v_lshl_add_u64 v[192:193], s[16:17], 0, v[0:1]
	global_load_lds_dwordx4 v0, s[16:17]
	s_mov_b32 m0, s72
	s_nop 0
	global_load_lds_dwordx4 v144, s[16:17]
	v_lshl_add_u64 v[144:145], s[16:17], 0, v[144:145]
	s_barrier
	s_add_i32 s20, 0, 0x18000
	v_add_u32_e32 v0, s20, v147
	s_add_i32 s21, 0, 0x1c000
	ds_read_b128 v[150:153], v0
	ds_read_b128 v[154:157], v0 offset:1024
	ds_read_b128 v[158:161], v0 offset:2048
	ds_read_b128 v[162:165], v0 offset:3072
	v_add_u32_e32 v0, s21, v147
	ds_read_b128 v[166:169], v0
	ds_read_b128 v[170:173], v0 offset:1024
	ds_read_b128 v[174:177], v0 offset:2048
	ds_read_b128 v[178:181], v0 offset:3072
	s_mov_b32 m0, s73
	v_lshl_add_u64 v[142:143], s[16:17], 0, v[142:143]
	ds_read_b128 v[182:185], v148 offset:32768
	ds_read_b128 v[202:205], v148 offset:33792
	ds_read_b128 v[206:209], v148 offset:34816
	ds_read_b128 v[214:217], v148 offset:35840
	ds_read_b128 v[218:221], v148 offset:36864
	ds_read_b128 v[222:225], v148 offset:37888
	ds_read_b128 v[226:229], v148 offset:38912
	ds_read_b128 v[230:233], v148 offset:39936
	global_load_lds_dwordx4 v[142:143], off
	v_lshl_add_u64 v[140:141], s[16:17], 0, v[140:141]
	s_mov_b32 m0, s90
	s_nop 0
	global_load_lds_dwordx4 v[140:141], off
	s_waitcnt vmcnt(8)
	s_waitcnt lgkmcnt(0)
	s_barrier
; #define PG8_STAGE(bufoff, gbase, voff) do { _Pragma("unroll") for (int _i = 0; _i < 2; ++_i) \
;         __builtin_amdgcn_global_load_lds((const unsigned*)((const char*)(gbase) + (voff)[_i]), (LAS unsigned*)(lds + (bufoff) + ldsw + _i * 8192), 16, 0, 0); } while (0)
; #define PG8_LDA(dst, b, h) do { _Pragma("unroll") for (int m = 0; m < 4; ++m) _Pragma("unroll") for (int k = 0; k < 2; ++k) dst[m][k] = *(const LAS bf16x8*)(lds + PG8_SA(b, h) + aoff + m * 2048 + k * 1024); } while (0)
; #define PG8_MMA(ai, bj, At, Bt) do { __builtin_amdgcn_s_setprio(1); _Pragma("unroll") for (int m = 0; m < 4; ++m) _Pragma("unroll") for (int n = 0; n < 2; ++n) _Pragma("unroll") for (int k = 0; k < 2; ++k) \
;         acc[ai][bj][m][n] = __builtin_amdgcn_mfma_f32_16x16x32_bf16(Bt[n][k], At[m][k], acc[ai][bj][m][n], 0, 0, 0); __builtin_amdgcn_s_setprio(0); } while (0)
; #define PG8_WAIT_V(n) asm volatile("s_waitcnt vmcnt(" #n ")" ::: "memory")
; #define PG8_WAIT_L(n) asm volatile("s_waitcnt lgkmcnt(" #n ")" ::: "memory")
; #define PG8_BAR __builtin_amdgcn_s_barrier()
; #define PG8_SCHED __builtin_amdgcn_sched_barrier(0)
; template <class Epi, class Sched>
; __device__ __forceinline__ void gemm_phase(LAS unsigned char* lds, const int tid, const char* Abase, const int K, const Sched& S, const Epi& E) {
;     ...
;             PG8_WAIT_V(8); PG8_WAIT_L(0); PG8_BAR; PG8_MMA(0, 0, At, B0); PG8_MMA(0, 1, At, B1); PG8_BAR; PG8_SCHED;
;             PG8_LDA(At, 1, 1); PG8_STAGE(PG8_SB(1, 0), b3, voffB); PG8_STAGE(PG8_SB(1, 1), b3 + hstep, voffB); PG8_STAGE(PG8_SA(1, 0), a3, w2[0]);
;             PG8_WAIT_V(8); PG8_WAIT_L(0); PG8_BAR; PG8_MMA(1, 0, At, B0); PG8_MMA(1, 1, At, B1); PG8_BAR; PG8_SCHED;
;         }
	s_setprio 1
	s_waitcnt lgkmcnt(0)
	v_mfma_f32_16x16x32_bf16 v[130:133], v[150:153], v[182:185], v[130:133]
	v_mfma_f32_16x16x32_bf16 v[126:129], v[158:161], v[182:185], v[126:129]
	v_mfma_f32_16x16x32_bf16 v[110:113], v[150:153], v[206:209], v[110:113]
	v_mfma_f32_16x16x32_bf16 v[106:109], v[158:161], v[206:209], v[106:109]
	v_mfma_f32_16x16x32_bf16 v[94:97], v[150:153], v[218:221], v[94:97]
	v_mfma_f32_16x16x32_bf16 v[90:93], v[158:161], v[218:221], v[90:93]
	v_mfma_f32_16x16x32_bf16 v[78:81], v[150:153], v[226:229], v[78:81]
	v_mfma_f32_16x16x32_bf16 v[74:77], v[158:161], v[226:229], v[74:77]
	v_mfma_f32_16x16x32_bf16 v[130:133], v[154:157], v[202:205], v[130:133]
	v_mfma_f32_16x16x32_bf16 v[126:129], v[162:165], v[202:205], v[126:129]
	v_mfma_f32_16x16x32_bf16 v[110:113], v[154:157], v[214:217], v[110:113]
	v_mfma_f32_16x16x32_bf16 v[106:109], v[162:165], v[214:217], v[106:109]
	v_mfma_f32_16x16x32_bf16 v[94:97], v[154:157], v[222:225], v[94:97]
	v_mfma_f32_16x16x32_bf16 v[90:93], v[162:165], v[222:225], v[90:93]
	v_mfma_f32_16x16x32_bf16 v[78:81], v[154:157], v[230:233], v[78:81]
	v_mfma_f32_16x16x32_bf16 v[74:77], v[162:165], v[230:233], v[74:77]
	s_setprio 0
	s_setprio 1
	v_mfma_f32_16x16x32_bf16 v[122:125], v[166:169], v[182:185], v[122:125]
	v_mfma_f32_16x16x32_bf16 v[118:121], v[174:177], v[182:185], v[118:121]
	v_mfma_f32_16x16x32_bf16 v[102:105], v[166:169], v[206:209], v[102:105]
	v_mfma_f32_16x16x32_bf16 v[98:101], v[174:177], v[206:209], v[98:101]
	v_mfma_f32_16x16x32_bf16 v[86:89], v[166:169], v[218:221], v[86:89]
	v_mfma_f32_16x16x32_bf16 v[82:85], v[174:177], v[218:221], v[82:85]
	v_mfma_f32_16x16x32_bf16 v[70:73], v[166:169], v[226:229], v[70:73]
	v_mfma_f32_16x16x32_bf16 v[66:69], v[174:177], v[226:229], v[66:69]
	v_mfma_f32_16x16x32_bf16 v[122:125], v[170:173], v[202:205], v[122:125]
	v_mfma_f32_16x16x32_bf16 v[118:121], v[178:181], v[202:205], v[118:121]
	v_mfma_f32_16x16x32_bf16 v[102:105], v[170:173], v[214:217], v[102:105]
	v_mfma_f32_16x16x32_bf16 v[98:101], v[178:181], v[214:217], v[98:101]
	v_mfma_f32_16x16x32_bf16 v[86:89], v[170:173], v[222:225], v[86:89]
	v_mfma_f32_16x16x32_bf16 v[82:85], v[178:181], v[222:225], v[82:85]
	v_mfma_f32_16x16x32_bf16 v[70:73], v[170:173], v[230:233], v[70:73]
	v_mfma_f32_16x16x32_bf16 v[66:69], v[178:181], v[230:233], v[66:69]
	s_setprio 0
	s_barrier
	s_add_i32 s16, s20, s70
	v_lshl_add_u64 v[186:187], v[186:187], 0, s[24:25]
	s_mov_b32 m0, s16
	ds_read_b128 v[140:143], v148 offset:49152
	ds_read_b128 v[182:185], v148 offset:50176
	ds_read_b128 v[202:205], v148 offset:51200
	ds_read_b128 v[206:209], v148 offset:52224
	ds_read_b128 v[214:217], v148 offset:53248
	ds_read_b128 v[218:221], v148 offset:54272
	ds_read_b128 v[222:225], v148 offset:55296
	ds_read_b128 v[226:229], v148 offset:56320
	global_load_lds_dwordx4 v[186:187], off
	s_add_i32 m0, s16, 0x2000
	s_add_u32 s14, s14, 0x40080
	v_lshl_add_u64 v[186:187], v[190:191], 0, s[24:25]
	s_addc_u32 s15, s15, 0
	s_add_i32 s16, s21, s70
	global_load_lds_dwordx4 v[186:187], off
	s_waitcnt vmcnt(4)
	s_waitcnt lgkmcnt(0)
	s_barrier
	s_setprio 1
	s_waitcnt lgkmcnt(0)
	v_mfma_f32_16x16x32_bf16 v[62:65], v[150:153], v[140:143], v[62:65]
	v_mfma_f32_16x16x32_bf16 v[58:61], v[158:161], v[140:143], v[58:61]
	v_mfma_f32_16x16x32_bf16 v[46:49], v[150:153], v[202:205], v[46:49]
	v_mfma_f32_16x16x32_bf16 v[42:45], v[158:161], v[202:205], v[42:45]
	v_mfma_f32_16x16x32_bf16 v[30:33], v[150:153], v[214:217], v[30:33]
	v_mfma_f32_16x16x32_bf16 v[26:29], v[158:161], v[214:217], v[26:29]
	v_mfma_f32_16x16x32_bf16 v[14:17], v[150:153], v[222:225], v[14:17]
	v_mfma_f32_16x16x32_bf16 v[10:13], v[158:161], v[222:225], v[10:13]
	v_mfma_f32_16x16x32_bf16 v[62:65], v[154:157], v[182:185], v[62:65]
	v_mfma_f32_16x16x32_bf16 v[58:61], v[162:165], v[182:185], v[58:61]
	v_mfma_f32_16x16x32_bf16 v[46:49], v[154:157], v[206:209], v[46:49]
	v_mfma_f32_16x16x32_bf16 v[42:45], v[162:165], v[206:209], v[42:45]
	v_mfma_f32_16x16x32_bf16 v[30:33], v[154:157], v[218:221], v[30:33]
	v_mfma_f32_16x16x32_bf16 v[26:29], v[162:165], v[218:221], v[26:29]
	v_mfma_f32_16x16x32_bf16 v[14:17], v[154:157], v[226:229], v[14:17]
	v_mfma_f32_16x16x32_bf16 v[10:13], v[162:165], v[226:229], v[10:13]
	s_setprio 0
	s_setprio 1
	v_mfma_f32_16x16x32_bf16 v[54:57], v[166:169], v[140:143], v[54:57]
	v_mfma_f32_16x16x32_bf16 v[50:53], v[174:177], v[140:143], v[50:53]
	v_mfma_f32_16x16x32_bf16 v[38:41], v[166:169], v[202:205], v[38:41]
	v_mfma_f32_16x16x32_bf16 v[34:37], v[174:177], v[202:205], v[34:37]
	v_mfma_f32_16x16x32_bf16 v[22:25], v[166:169], v[214:217], v[22:25]
	v_mfma_f32_16x16x32_bf16 v[18:21], v[174:177], v[214:217], v[18:21]
	v_mfma_f32_16x16x32_bf16 v[6:9], v[166:169], v[222:225], v[6:9]
	v_mfma_f32_16x16x32_bf16 v[2:5], v[174:177], v[222:225], v[2:5]
	v_mfma_f32_16x16x32_bf16 v[54:57], v[170:173], v[182:185], v[54:57]
	v_mfma_f32_16x16x32_bf16 v[50:53], v[178:181], v[182:185], v[50:53]
	v_mfma_f32_16x16x32_bf16 v[38:41], v[170:173], v[206:209], v[38:41]
	v_mfma_f32_16x16x32_bf16 v[34:37], v[178:181], v[206:209], v[34:37]
	v_mfma_f32_16x16x32_bf16 v[22:25], v[170:173], v[218:221], v[22:25]
	v_mfma_f32_16x16x32_bf16 v[18:21], v[178:181], v[218:221], v[18:21]
	v_mfma_f32_16x16x32_bf16 v[6:9], v[170:173], v[226:229], v[6:9]
	v_mfma_f32_16x16x32_bf16 v[2:5], v[178:181], v[226:229], v[2:5]
	s_setprio 0
	v_lshl_add_u64 v[186:187], s[14:15], 0, v[134:135]
	s_mov_b32 m0, s16
	v_lshl_add_u64 v[144:145], v[144:145], 0, s[24:25]
	global_load_lds_dwordx4 v[186:187], off
	v_lshl_add_u64 v[186:187], s[14:15], 0, v[136:137]
	s_add_i32 m0, s16, 0x2000
	s_nop 0
	global_load_lds_dwordx4 v[186:187], off
	v_lshl_add_u64 v[186:187], v[192:193], 0, s[24:25]
	s_mov_b32 m0, s2
	s_nop 0
	global_load_lds_dwordx4 v[186:187], off
	s_mov_b32 m0, s33
	s_nop 0
	global_load_lds_dwordx4 v[144:145], off
	s_barrier
	s_add_i32 s19, s19, 2
	s_add_u32 s7, s7, 0x100
	s_addc_u32 s18, s18, 0
	s_add_u32 s12, s12, 0x100
	s_addc_u32 s13, s13, 0
	s_cmp_gt_u32 s19, 13
	s_cbranch_scc1 .LBB0_350
